# loop-edge edit: per-tile wait selection falls through on the common path, rare tail wait moved out of line (on top of LDS-DMA staging of 16 Wv fragments)
# baseline (speedup 1.0000x reference)
.Lring_tile_0:
	s_cmp_lt_u32 s30, 22
	s_cbranch_scc0 .Lring_w0_0
	s_waitcnt vmcnt(27)

.Lring_w0_0:
	s_waitcnt vmcnt(0)
	s_branch .Lring_go_0
